# speedup vs baseline: 1.0074x; 1.0074x over previous
_Z8k_stageAPKfS0_S0_S0_PDF16_PKDF16_S0_S1_ii:
	s_load_dwordx2 s[64:65], s[0:1], 0x40
	v_readfirstlane_b32 s94, v0
	s_nop 0
	s_lshr_b32 s94, s94, 6
	s_load_dwordx8 s[4:11], s[0:1], 0x0
	v_readfirstlane_b32 s14, v0
	s_lshr_b32 s15, s2, 5
	s_lshl_b32 s2, s2, 7
	s_lshr_b32 s20, s14, 6
	s_and_b32 s12, s2, 0xf80
	s_lshl_b32 s13, s15, 12
	s_mov_b32 s18, s3
	s_cmpk_lt_u32 s14, 0x100
	s_waitcnt lgkmcnt(0)
	s_cselect_b32 s2, s4, s6
	s_cselect_b32 s3, s5, s7
	s_cselect_b32 s4, s8, s10
	s_cselect_b32 s5, s9, s11
	s_cmp_eq_u32 s18, 0
	s_cselect_b32 s3, s3, s5
	s_cselect_b32 s2, s2, s4
	s_lshr_b32 s5, s14, 1
	s_lshl_b32 s4, s15, 7
	s_and_b32 s5, s5, 0x60
	v_bfe_u32 v1, v0, 5, 1
	s_or_b32 s4, s5, s4
	v_lshl_or_b32 v82, v1, 3, s4
	v_mov_b32_e32 v83, 0
	v_lshlrev_b64 v[2:3], 14, v[82:83]
	v_lshlrev_b32_e32 v78, 2, v0
	s_mov_b32 s17, 0
	v_lshl_add_u64 v[2:3], s[2:3], 0, v[2:3]
	s_lshl_b32 s16, s12, 2
	v_and_b32_e32 v79, 0x7c, v78
	v_lshl_add_u64 v[2:3], v[2:3], 0, s[16:17]
	v_lshlrev_b32_e32 v82, 2, v79
	v_lshl_add_u64 v[42:43], v[2:3], 0, v[82:83]
	s_movk_i32 s21, 0x4000
	v_add_co_u32_e32 v10, vcc, s21, v42
	s_mov_b32 s2, 0x8000
	s_nop 0
	v_addc_co_u32_e32 v11, vcc, 0, v43, vcc
	v_add_co_u32_e32 v18, vcc, s2, v42
	s_mov_b32 s2, 0xc000
	s_nop 0
	v_addc_co_u32_e32 v19, vcc, 0, v43, vcc
	v_add_co_u32_e32 v20, vcc, s2, v42
	s_mov_b32 s14, 0x10000
	s_nop 0
	v_addc_co_u32_e32 v21, vcc, 0, v43, vcc
	v_add_co_u32_e32 v26, vcc, s14, v42
	s_mov_b32 s2, 0x14000
	s_nop 0
	v_addc_co_u32_e32 v27, vcc, 0, v43, vcc
	v_add_co_u32_e32 v28, vcc, s2, v42
	s_mov_b32 s2, 0x18000
	s_nop 0
	v_addc_co_u32_e32 v29, vcc, 0, v43, vcc
	v_add_co_u32_e32 v34, vcc, s2, v42
	s_mov_b32 s2, 0x1c000
	s_nop 0
	v_addc_co_u32_e32 v35, vcc, 0, v43, vcc
	v_add_co_u32_e32 v36, vcc, s2, v42
	s_mov_b32 s2, 0x40000
	s_nop 0
	v_addc_co_u32_e32 v37, vcc, 0, v43, vcc
	v_add_co_u32_e32 v66, vcc, s2, v42
	s_mov_b32 s2, 0x44000
	s_nop 0
	v_addc_co_u32_e32 v67, vcc, 0, v43, vcc
	v_add_co_u32_e32 v68, vcc, s2, v42
	s_mov_b32 s2, 0x48000
	s_nop 0
	v_addc_co_u32_e32 v69, vcc, 0, v43, vcc
	global_load_dwordx4 v[2:5], v[42:43], off nt
	global_load_dwordx4 v[6:9], v[10:11], off nt
	v_add_co_u32_e32 v44, vcc, s2, v42
	global_load_dwordx4 v[10:13], v[18:19], off nt
	global_load_dwordx4 v[14:17], v[20:21], off nt
	s_nop 0
	global_load_dwordx4 v[18:21], v[26:27], off nt
	global_load_dwordx4 v[22:25], v[28:29], off nt
	s_nop 0
	global_load_dwordx4 v[26:29], v[34:35], off nt
	global_load_dwordx4 v[30:33], v[36:37], off nt
	v_addc_co_u32_e32 v45, vcc, 0, v43, vcc
	s_mov_b32 s2, 0x4c000
	v_add_co_u32_e32 v46, vcc, s2, v42
	s_mov_b32 s2, 0x50000
	s_nop 0
	v_addc_co_u32_e32 v47, vcc, 0, v43, vcc
	v_add_co_u32_e32 v70, vcc, s2, v42
	s_mov_b32 s2, 0x54000
	s_nop 0
	v_addc_co_u32_e32 v71, vcc, 0, v43, vcc
	v_add_co_u32_e32 v72, vcc, s2, v42
	s_mov_b32 s2, 0x58000
	s_nop 0
	v_addc_co_u32_e32 v73, vcc, 0, v43, vcc
	v_add_co_u32_e32 v74, vcc, s2, v42
	s_mov_b32 s2, 0x5c000
	s_nop 0
	v_addc_co_u32_e32 v75, vcc, 0, v43, vcc
	v_add_co_u32_e32 v76, vcc, s2, v42
	global_load_dwordx4 v[34:37], v[44:45], off nt
	global_load_dwordx4 v[38:41], v[46:47], off nt
	v_addc_co_u32_e32 v77, vcc, 0, v43, vcc
	global_load_dwordx4 v[42:45], v[74:75], off nt
	global_load_dwordx4 v[46:49], v[76:77], off nt
	global_load_dwordx4 v[50:53], v[70:71], off nt
	global_load_dwordx4 v[54:57], v[72:73], off nt
	global_load_dwordx4 v[58:61], v[66:67], off nt
	global_load_dwordx4 v[62:65], v[68:69], off nt
	v_lshl_or_b32 v1, s20, 2, v1
	v_lshrrev_b32_e32 v70, 5, v0
	v_or_b32_e32 v141, 0x200, v0
	v_or_b32_e32 v142, 0x600, v0
	s_or_b32 s16, s13, s12
	s_ashr_i32 s19, s18, 31
	s_lshl_b64 s[12:13], s[16:17], 9
	s_mov_b32 s15, 0x20000
	v_or_b32_e32 v144, 0xa00, v0
	v_bfe_u32 v140, v0, 4, 2
	v_and_b32_e32 v145, 15, v0
	v_lshlrev_b32_e32 v220, 9, v145
	s_waitcnt vmcnt(14)
	v_cvt_pk_f16_f32 v66, v2, v6
	v_lshlrev_b32_e32 v6, 9, v79
	v_bitop3_b32 v2, v78, v1, 12 bitop3:0x6c
	s_waitcnt vmcnt(12)
	v_cvt_pk_f16_f32 v67, v10, v14
	s_waitcnt vmcnt(10)
	v_cvt_pk_f16_f32 v68, v18, v22
	s_waitcnt vmcnt(8)
	v_cvt_pk_f16_f32 v69, v26, v30
	v_lshl_add_u32 v2, v2, 4, v6
	ds_write_b128 v2, v[66:69]
	v_cvt_pk_f16_f32 v66, v3, v7
	v_or_b32_e32 v7, 1, v79
	v_lshlrev_b32_e32 v10, 9, v7
	v_bitop3_b32 v2, v7, v1, 13 bitop3:0x6c
	v_cvt_pk_f16_f32 v69, v27, v31
	v_cvt_pk_f16_f32 v68, v19, v23
	v_cvt_pk_f16_f32 v67, v11, v15
	v_lshl_add_u32 v2, v2, 4, v10
	ds_write_b128 v2, v[66:69]
	v_cvt_pk_f16_f32 v66, v4, v8
	v_or_b32_e32 v8, 2, v79
	v_lshlrev_b32_e32 v11, 9, v8
	v_bitop3_b32 v2, v8, v1, 14 bitop3:0x6c
	v_cvt_pk_f16_f32 v69, v28, v32
	v_cvt_pk_f16_f32 v68, v20, v24
	v_cvt_pk_f16_f32 v67, v12, v16
	v_lshl_add_u32 v2, v2, 4, v11
	v_cvt_pk_f16_f32 v12, v5, v9
	v_or_b32_e32 v9, 3, v79
	ds_write_b128 v2, v[66:69]
	v_lshlrev_b32_e32 v16, 9, v9
	v_bitop3_b32 v2, v9, v1, 15 bitop3:0x6c
	v_cvt_pk_f16_f32 v15, v29, v33
	v_cvt_pk_f16_f32 v14, v21, v25
	v_cvt_pk_f16_f32 v13, v13, v17
	v_lshl_add_u32 v2, v2, 4, v16
	v_or_b32_e32 v1, 2, v1
	ds_write_b128 v2, v[12:15]
	v_bitop3_b32 v12, v78, v1, 12 bitop3:0x6c
	s_waitcnt vmcnt(4)
	v_cvt_pk_f16_f32 v5, v42, v46
	s_waitcnt vmcnt(2)
	v_cvt_pk_f16_f32 v4, v50, v54
	v_cvt_pk_f16_f32 v3, v34, v38
	s_waitcnt vmcnt(0)
	v_cvt_pk_f16_f32 v2, v58, v62
	v_lshl_add_u32 v6, v12, 4, v6
	ds_write_b128 v6, v[2:5]
	v_bitop3_b32 v6, v7, v1, 13 bitop3:0x6c
	v_cvt_pk_f16_f32 v5, v43, v47
	v_cvt_pk_f16_f32 v4, v51, v55
	v_cvt_pk_f16_f32 v3, v35, v39
	v_cvt_pk_f16_f32 v2, v59, v63
	v_lshl_add_u32 v6, v6, 4, v10
	ds_write_b128 v6, v[2:5]
	v_bitop3_b32 v6, v8, v1, 14 bitop3:0x6c
	v_cvt_pk_f16_f32 v5, v44, v48
	v_cvt_pk_f16_f32 v4, v52, v56
	v_cvt_pk_f16_f32 v3, v36, v40
	v_cvt_pk_f16_f32 v2, v60, v64
	v_lshl_add_u32 v6, v6, 4, v11
	v_bitop3_b32 v1, v9, v1, 15 bitop3:0x6c
	ds_write_b128 v6, v[2:5]
	v_cvt_pk_f16_f32 v5, v45, v49
	v_cvt_pk_f16_f32 v4, v53, v57
	v_cvt_pk_f16_f32 v3, v37, v41
	v_cvt_pk_f16_f32 v2, v61, v65
	v_lshl_add_u32 v1, v1, 4, v16
	ds_write_b128 v1, v[2:5]
	v_bitop3_b32 v2, v70, v0, 31 bitop3:0x78
	v_lshlrev_b32_e32 v1, 9, v70
	v_lshlrev_b32_e32 v22, 4, v2
	v_or_b32_e32 v10, v22, v1
	s_waitcnt lgkmcnt(0)
	s_barrier
	ds_read_b128 v[2:5], v10
	s_load_dwordx8 s[4:11], s[0:1], 0x20
	s_load_dwordx2 s[2:3], s[0:1], 0x40
	v_lshlrev_b32_e32 v24, 4, v0
	v_and_b32_e32 v25, 0x1e00, v24
	v_or_b32_e32 v26, v22, v25
	s_waitcnt lgkmcnt(0)
	v_pk_max_f16 v6, v5, v5
	v_and_b32_e32 v18, 31, v0
	v_pk_max_f16 v9, v6, 0
	v_pk_max_f16 v6, v4, v4
	v_lshlrev_b32_e32 v29, 4, v18
	v_pk_max_f16 v8, v6, 0
	v_pk_max_f16 v6, v3, v3
	s_lshl_b64 s[0:1], s[18:19], 23
	v_pk_max_f16 v7, v6, 0
	v_pk_max_f16 v6, v2, v2
	s_add_u32 s0, s4, s0
	v_pk_max_f16 v6, v6, 0
	ds_write_b128 v10, v[6:9]
	v_lshlrev_b32_e32 v6, 4, v141
	v_and_b32_e32 v23, 0x3e00, v6
	v_or_b32_e32 v14, v22, v23
	ds_read_b128 v[6:9], v14
	s_addc_u32 s1, s5, s1
	s_add_u32 s12, s0, s12
	s_addc_u32 s0, s1, s13
	s_and_b32 s13, s0, 0xffff
	s_waitcnt lgkmcnt(0)
	v_pk_max_f16 v10, v9, v9
	v_or_b32_e32 v1, v1, v29
	v_pk_max_f16 v13, v10, 0
	v_pk_max_f16 v10, v8, v8
	buffer_store_dwordx4 v[2:5], v1, s[12:15], 0 offen sc1
	v_pk_max_f16 v12, v10, 0
	v_pk_max_f16 v10, v7, v7
	v_or_b32_e32 v1, v23, v29
	v_pk_max_f16 v11, v10, 0
	v_pk_max_f16 v10, v6, v6
	buffer_store_dwordx4 v[6:9], v1, s[12:15], 0 offen sc1
	v_pk_max_f16 v10, v10, 0
	ds_write_b128 v14, v[10:13]
	ds_read_b128 v[10:13], v26 offset:16384
	v_or_b32_e32 v25, v25, v29
	v_or_b32_e32 v6, 0x4000, v25
	s_mov_b32 s0, 0xfe00
	s_waitcnt lgkmcnt(0)
	v_pk_max_f16 v14, v13, v13
	s_nop 0
	v_pk_max_f16 v17, v14, 0
	v_pk_max_f16 v14, v12, v12
	buffer_store_dwordx4 v[10:13], v6, s[12:15], 0 offen sc1
	v_pk_max_f16 v16, v14, 0
	v_pk_max_f16 v14, v11, v11
	s_nop 0
	v_pk_max_f16 v15, v14, 0
	v_pk_max_f16 v14, v10, v10
	s_nop 0
	v_pk_max_f16 v14, v14, 0
	ds_write_b128 v26, v[14:17] offset:16384
	v_lshlrev_b32_e32 v14, 4, v142
	v_and_b32_e32 v27, 0x7e00, v14
	v_or_b32_e32 v28, v22, v27
	ds_read_b128 v[14:17], v28
	v_or_b32_e32 v10, v27, v29
	s_waitcnt lgkmcnt(0)
	v_pk_max_f16 v18, v17, v17
	s_nop 0
	v_pk_max_f16 v21, v18, 0
	v_pk_max_f16 v18, v16, v16
	buffer_store_dwordx4 v[14:17], v10, s[12:15], 0 offen sc1
	v_pk_max_f16 v20, v18, 0
	v_pk_max_f16 v18, v15, v15
	v_or_b32_e32 v10, 0x8000, v25
	v_pk_max_f16 v19, v18, 0
	v_pk_max_f16 v18, v14, v14
	s_nop 0
	v_pk_max_f16 v18, v18, 0
	ds_write_b128 v28, v[18:21]
	ds_read_b128 v[18:21], v26 offset:32768
	s_waitcnt lgkmcnt(0)
	v_pk_max_f16 v1, v21, v21
	s_nop 0
	v_pk_max_f16 v5, v1, 0
	v_pk_max_f16 v1, v20, v20
	buffer_store_dwordx4 v[18:21], v10, s[12:15], 0 offen sc1
	v_pk_max_f16 v4, v1, 0
	v_pk_max_f16 v1, v19, v19
	s_nop 0
	v_pk_max_f16 v3, v1, 0
	v_pk_max_f16 v1, v18, v18
	s_nop 0
	v_pk_max_f16 v2, v1, 0
	v_lshlrev_b32_e32 v1, 4, v144
	v_and_b32_e32 v1, 0xbe00, v1
	ds_write_b128 v26, v[2:5] offset:32768
	v_or_b32_e32 v23, v22, v1
	ds_read_b128 v[2:5], v23
	v_or_b32_e32 v1, v1, v29
	s_waitcnt lgkmcnt(0)
	v_pk_max_f16 v6, v5, v5
	s_nop 0
	v_pk_max_f16 v9, v6, 0
	v_pk_max_f16 v6, v4, v4
	buffer_store_dwordx4 v[2:5], v1, s[12:15], 0 offen sc1
	v_pk_max_f16 v8, v6, 0
	v_pk_max_f16 v6, v3, v3
	v_or_b32_e32 v1, 0xc000, v25
	v_pk_max_f16 v7, v6, 0
	v_pk_max_f16 v6, v2, v2
	s_nop 0
	v_pk_max_f16 v6, v6, 0
	ds_write_b128 v23, v[6:9]
	ds_read_b128 v[6:9], v26 offset:49152
	s_waitcnt lgkmcnt(0)
	v_pk_max_f16 v10, v9, v9
	s_nop 0
	v_pk_max_f16 v13, v10, 0
	v_pk_max_f16 v10, v8, v8
	buffer_store_dwordx4 v[6:9], v1, s[12:15], 0 offen sc1
	v_pk_max_f16 v12, v10, 0
	v_pk_max_f16 v10, v7, v7
	s_nop 0
	v_pk_max_f16 v11, v10, 0
	v_pk_max_f16 v10, v6, v6
	s_nop 0
	v_pk_max_f16 v10, v10, 0
	ds_write_b128 v26, v[10:13] offset:49152
	v_mov_b32_e32 v10, 0xe000
	v_bitop3_b32 v14, v24, s0, v10 bitop3:0xc8
	s_mul_i32 s0, s3, s18
	v_or_b32_e32 v15, v22, v14
	s_add_i32 s0, s0, s2
	ds_read_b128 v[10:13], v15
	s_mul_i32 s2, s0, 0x60000
	s_mul_hi_i32 s1, s0, 0x60000
	s_add_u32 s2, s6, s2
	s_mulk_i32 s0, 0x300
	s_addc_u32 s3, s7, s1
	s_ashr_i32 s1, s0, 31
	s_lshl_b64 s[0:1], s[0:1], 2
	v_or_b32_e32 v1, v14, v29
	s_add_u32 s4, s8, s0
	s_waitcnt lgkmcnt(0)
	buffer_store_dwordx4 v[10:13], v1, s[12:15], 0 offen sc1
	v_pk_max_f16 v1, v13, v13
	s_addc_u32 s5, s9, s1
	s_mul_i32 s0, s18, 0x1800000
	v_pk_max_f16 v5, v1, 0
	v_pk_max_f16 v1, v12, v12
	s_mul_hi_i32 s1, s18, 0x1800000
	s_add_u32 s0, s10, s0
	v_pk_max_f16 v4, v1, 0
	v_pk_max_f16 v1, v11, v11
	s_addc_u32 s1, s11, s1
	v_pk_max_f16 v3, v1, 0
	v_pk_max_f16 v1, v10, v10
	s_and_b32 s1, s1, 0xffff
	s_mul_i32 s7, s20, 0x6000
	v_pk_max_f16 v2, v1, 0
	v_and_b32_e32 v1, 63, v0
	s_mul_hi_u32 s6, s20, 0x6000
	s_add_u32 s2, s2, s7
	s_addc_u32 s3, s3, s6
	v_lshlrev_b32_e32 v82, 4, v1
	v_lshl_add_u64 v[118:119], s[2:3], 0, v[82:83]
	s_movk_i32 s6, 0x1000
	v_add_co_u32_e32 v50, vcc, s6, v118
	s_movk_i32 s6, 0x2000
	s_nop 0
	v_addc_co_u32_e32 v51, vcc, 0, v119, vcc
	ds_write_b128 v15, v[2:5]
	v_add_co_u32_e32 v52, vcc, s6, v118
	global_load_dwordx4 v[2:5], v82, s[2:3] offset:1024
	global_load_dwordx4 v[6:9], v82, s[2:3] offset:2048
	v_addc_co_u32_e32 v53, vcc, 0, v119, vcc
	global_load_dwordx4 v[10:13], v82, s[2:3] offset:3072
	global_load_dwordx4 v[14:17], v[52:53], off offset:-4096
	global_load_dwordx4 v[18:21], v[50:51], off offset:1024
	global_load_dwordx4 v[22:25], v[50:51], off offset:2048
	global_load_dwordx4 v[26:29], v82, s[2:3]
	global_load_dwordx4 v[30:33], v[50:51], off offset:3072
	global_load_dwordx4 v[34:37], v[52:53], off
	global_load_dwordx4 v[38:41], v[52:53], off offset:1024
	global_load_dwordx4 v[42:45], v[52:53], off offset:2048
	global_load_dwordx4 v[46:49], v[52:53], off offset:3072
	s_movk_i32 s2, 0x3000
	v_add_co_u32_e32 v116, vcc, s2, v118
	s_waitcnt lgkmcnt(0)
	s_nop 0
	v_addc_co_u32_e32 v117, vcc, 0, v119, vcc
	v_add_co_u32_e32 v132, vcc, s21, v118
	s_barrier
	s_cmp_lt_u32 s94, 4
	s_cbranch_scc1 .Lmystag1_2
	s_sleep 7

_Z7k_stageILi0ELi8EEv8AttnArgsPKDF16_PKfPDF16_iii:
	s_load_dwordx16 s[64:79], s[0:1], 0x40
	s_load_dwordx16 s[64:79], s[0:1], 0x0
	v_readfirstlane_b32 s94, v0
	s_nop 0
	s_lshr_b32 s94, s94, 6
	s_load_dwordx4 s[8:11], s[0:1], 0x88
	s_lshl_b32 s4, s2, 4
	s_and_b32 s4, s4, 0x70
	s_lshr_b32 s5, s2, 3
	s_add_i32 s4, s4, s5
	s_lshr_b32 s7, s4, 5
	s_lshl_b32 s6, s4, 1
	s_waitcnt lgkmcnt(0)
	s_lshl_b32 s11, s2, 1
	s_cmp_gt_i32 s10, 0
	v_readfirstlane_b32 s24, v0
	s_cbranch_scc1 .LBB3_2
	s_lshl_b32 s31, s7, 12
	s_ashr_i32 s2, s3, 31
	s_mov_b64 s[4:5], 0
	s_branch .LBB3_3
